# v16 + nontemporal X1 stores in the LayerNorm-1 phase
# speedup vs baseline: 1.0135x; 1.0004x over previous
.LBB0_780:
	v_mov_b32_e32 v152, v196
	s_waitcnt vmcnt(31)
	v_lshlrev_b32_e32 v108, 16, v98
	v_lshl_add_u32 v153, v152, 4, 0
	v_add_u32_e32 v110, 0x20100, v153
	s_waitcnt lgkmcnt(0)
	ds_read_b128 v[102:105], v110
	ds_read_b128 v[112:115], v110 offset:1024
	v_and_b32_e32 v109, 0xffff0000, v98
	v_lshlrev_b32_e32 v98, 16, v99
	v_and_b32_e32 v99, 0xffff0000, v99
	s_waitcnt lgkmcnt(1)
	v_pk_mul_f32 v[102:103], v[102:103], v[108:109]
	v_pk_mul_f32 v[98:99], v[104:105], v[98:99]
	s_waitcnt vmcnt(30)
	v_pk_fma_f32 v[146:147], v[66:67], s[18:19], v[102:103] op_sel_hi:[1,0,1]
	s_waitcnt vmcnt(27)
	v_lshlrev_b32_e32 v66, 16, v100
	v_and_b32_e32 v67, 0xffff0000, v100
	v_pk_fma_f32 v[108:109], v[68:69], s[18:19], v[98:99] op_sel_hi:[1,0,1]
	v_lshlrev_b32_e32 v68, 16, v101
	v_and_b32_e32 v69, 0xffff0000, v101
	s_waitcnt lgkmcnt(0)
	v_pk_mul_f32 v[66:67], v[112:113], v[66:67]
	v_pk_mul_f32 v[68:69], v[114:115], v[68:69]
	s_waitcnt vmcnt(26)
	v_pk_fma_f32 v[144:145], v[70:71], s[18:19], v[66:67] op_sel_hi:[1,0,1]
	v_pk_fma_f32 v[142:143], v[72:73], s[18:19], v[68:69] op_sel_hi:[1,0,1]
	v_mov_b32_e32 v66, v144
	v_mov_b32_e32 v67, v146
	v_mov_b32_e32 v68, v145
	v_mov_b32_e32 v69, v147
	v_pk_add_f32 v[66:67], v[66:67], v[68:69]
	v_mov_b32_e32 v68, v142
	v_mov_b32_e32 v69, v108
	v_mov_b32_e32 v70, v143
	v_mov_b32_e32 v71, v109
	v_pk_add_f32 v[68:69], v[68:69], v[70:71]
	s_waitcnt vmcnt(23)
	v_lshlrev_b32_e32 v100, 16, v106
	v_pk_add_f32 v[66:67], v[66:67], v[68:69]
	v_and_b32_e32 v101, 0xffff0000, v106
	v_add_f32_e32 v67, 0, v67
	v_add_f32_e32 v99, v66, v67
	ds_read_b128 v[66:69], v110 offset:2048
	ds_read_b128 v[70:73], v110 offset:3072
	v_lshlrev_b32_e32 v102, 16, v107
	v_and_b32_e32 v103, 0xffff0000, v107
	s_mov_b32 s34, s19
	s_waitcnt lgkmcnt(1)
	v_pk_mul_f32 v[68:69], v[68:69], v[102:103]
	v_pk_mul_f32 v[66:67], v[66:67], v[100:101]
	s_waitcnt vmcnt(22)
	v_pk_fma_f32 v[138:139], v[76:77], s[18:19], v[68:69] op_sel_hi:[1,0,1]
	v_pk_fma_f32 v[136:137], v[74:75], s[18:19], v[66:67] op_sel_hi:[1,0,1]
	v_mov_b32_e32 v69, v139
	v_pk_mov_b32 v[66:67], v[136:137], v[138:139] op_sel:[1,0]
	v_mov_b32_e32 v68, v136
	v_pk_add_f32 v[66:67], v[66:67], v[68:69]
	s_waitcnt vmcnt(19)
	v_lshlrev_b32_e32 v68, 16, v117
	v_pk_add_f32 v[74:75], v[66:67], v[66:67] op_sel_hi:[0,1]
	v_lshlrev_b32_e32 v66, 16, v116
	v_and_b32_e32 v67, 0xffff0000, v116
	v_and_b32_e32 v69, 0xffff0000, v117
	s_waitcnt lgkmcnt(0)
	v_pk_mul_f32 v[66:67], v[70:71], v[66:67]
	v_pk_mul_f32 v[68:69], v[72:73], v[68:69]
	s_waitcnt vmcnt(18)
	v_pk_fma_f32 v[132:133], v[78:79], s[18:19], v[66:67] op_sel_hi:[1,0,1]
	v_pk_fma_f32 v[130:131], v[80:81], s[18:19], v[68:69] op_sel_hi:[1,0,1]
	ds_read_b128 v[66:69], v110 offset:4096
	ds_read_b128 v[70:73], v110 offset:5120
	s_waitcnt vmcnt(14)
	v_lshlrev_b32_e32 v80, 16, v122
	v_and_b32_e32 v81, 0xffff0000, v122
	v_lshlrev_b32_e32 v100, 16, v123
	v_and_b32_e32 v101, 0xffff0000, v123
	s_waitcnt lgkmcnt(1)
	v_pk_mul_f32 v[66:67], v[66:67], v[80:81]
	v_pk_mul_f32 v[68:69], v[68:69], v[100:101]
	v_pk_fma_f32 v[126:127], v[82:83], s[18:19], v[66:67] op_sel_hi:[1,0,1]
	v_pk_fma_f32 v[124:125], v[84:85], s[18:19], v[68:69] op_sel_hi:[1,0,1]
	v_add_f32_e32 v77, v132, v133
	v_add_f32_e32 v79, v130, v131
	v_mov_b32_e32 v76, v126
	v_mov_b32_e32 v78, v127
	v_mov_b32_e32 v74, v124
	v_mov_b32_e32 v98, v125
	v_pk_add_f32 v[66:67], v[76:77], v[78:79]
	v_pk_add_f32 v[68:69], v[74:75], v[98:99]
	s_waitcnt vmcnt(6)
	v_lshlrev_b32_e32 v78, 16, v134
	v_pk_add_f32 v[66:67], v[66:67], v[68:69]
	v_lshlrev_b32_e32 v68, 16, v129
	v_pk_add_f32 v[74:75], v[66:67], v[66:67] op_sel_hi:[0,1]
	v_lshlrev_b32_e32 v66, 16, v128
	v_and_b32_e32 v67, 0xffff0000, v128
	v_and_b32_e32 v69, 0xffff0000, v129
	s_waitcnt lgkmcnt(0)
	v_pk_mul_f32 v[68:69], v[72:73], v[68:69]
	v_pk_mul_f32 v[66:67], v[70:71], v[66:67]
	v_pk_fma_f32 v[120:121], v[88:89], s[18:19], v[68:69] op_sel_hi:[1,0,1]
	v_pk_fma_f32 v[118:119], v[86:87], s[18:19], v[66:67] op_sel_hi:[1,0,1]
	v_mov_b32_e32 v69, v121
	v_pk_mov_b32 v[66:67], v[118:119], v[120:121] op_sel:[1,0]
	v_mov_b32_e32 v68, v118
	v_pk_add_f32 v[66:67], v[66:67], v[68:69]
	ds_read_b128 v[70:73], v110 offset:7168
	v_pk_add_f32 v[76:77], v[66:67], v[66:67] op_sel_hi:[0,1]
	ds_read_b128 v[66:69], v110 offset:6144
	v_and_b32_e32 v79, 0xffff0000, v134
	v_lshlrev_b32_e32 v80, 16, v135
	v_and_b32_e32 v81, 0xffff0000, v135
	v_lshlrev_b32_e32 v82, 2, v152
	s_waitcnt lgkmcnt(0)
	v_pk_mul_f32 v[66:67], v[66:67], v[78:79]
	v_pk_mul_f32 v[68:69], v[68:69], v[80:81]
	s_waitcnt vmcnt(3)
	v_lshlrev_b32_e32 v78, 16, v140
	v_and_b32_e32 v79, 0xffff0000, v140
	v_lshlrev_b32_e32 v80, 16, v141
	v_and_b32_e32 v81, 0xffff0000, v141
	v_pk_mul_f32 v[70:71], v[70:71], v[78:79]
	v_pk_mul_f32 v[72:73], v[72:73], v[80:81]
	v_pk_fma_f32 v[112:113], v[92:93], s[18:19], v[68:69] op_sel_hi:[1,0,1]
	v_pk_fma_f32 v[114:115], v[90:91], s[18:19], v[66:67] op_sel_hi:[1,0,1]
	s_waitcnt vmcnt(2)
	v_pk_fma_f32 v[102:103], v[96:97], s[18:19], v[72:73] op_sel_hi:[1,0,1]
	v_pk_fma_f32 v[104:105], v[94:95], s[18:19], v[70:71] op_sel_hi:[1,0,1]
	v_add_f32_e32 v67, v114, v115
	v_add_f32_e32 v69, v112, v113
	v_mov_b32_e32 v66, v104
	v_mov_b32_e32 v68, v105
	v_mov_b32_e32 v76, v102
	v_mov_b32_e32 v74, v103
	v_pk_add_f32 v[66:67], v[66:67], v[68:69]
	v_pk_add_f32 v[68:69], v[76:77], v[74:75]
	s_add_i32 s19, s19, s24
	v_pk_add_f32 v[66:67], v[66:67], v[68:69]
	v_xor_b32_e32 v68, 32, v150
	v_add_f32_e32 v66, v66, v67
	v_and_b32_e32 v67, 64, v150
	v_add_u32_e32 v67, 64, v67
	v_cmp_lt_i32_e32 vcc, v68, v67
	s_cmpk_gt_i32 s19, 0x3fff
	s_cselect_b64 s[20:21], -1, 0
	v_cndmask_b32_e32 v68, v150, v68, vcc
	v_lshlrev_b32_e32 v154, 2, v68
	ds_bpermute_b32 v68, v154, v66
	s_cmpk_lt_i32 s19, 0x4000
	s_cselect_b64 s[22:23], -1, 0
	s_and_b64 s[0:1], s[22:23], exec
	v_add_u32_e32 v96, 0x22100, v153
	s_waitcnt lgkmcnt(0)
	v_add_f32_e32 v66, v66, v68
	v_xor_b32_e32 v68, 16, v150
	v_cmp_lt_i32_e32 vcc, v68, v67
	s_cselect_b32 s0, s19, s34
	v_add_u32_e32 v97, 0x24100, v153
	v_cndmask_b32_e32 v68, v150, v68, vcc
	v_lshlrev_b32_e32 v155, 2, v68
	ds_bpermute_b32 v68, v155, v66
	v_lshl_add_u32 v94, s0, 11, v82
	v_ashrrev_i32_e32 v95, 31, v94
	v_lshl_add_u64 v[78:79], v[94:95], 1, s[10:11]
	v_mov_b32_e32 v90, 0
	s_waitcnt lgkmcnt(0)
	v_add_f32_e32 v66, v66, v68
	v_xor_b32_e32 v68, 8, v150
	v_cmp_lt_i32_e32 vcc, v68, v67
	s_nop 1
	v_cndmask_b32_e32 v68, v150, v68, vcc
	v_lshlrev_b32_e32 v156, 2, v68
	ds_bpermute_b32 v68, v156, v66
	s_waitcnt lgkmcnt(0)
	v_add_f32_e32 v66, v66, v68
	v_xor_b32_e32 v68, 4, v150
	v_cmp_lt_i32_e32 vcc, v68, v67
	s_nop 1
	v_cndmask_b32_e32 v68, v150, v68, vcc
	v_lshlrev_b32_e32 v157, 2, v68
	ds_bpermute_b32 v68, v157, v66
	s_waitcnt lgkmcnt(0)
	v_add_f32_e32 v66, v66, v68
	v_xor_b32_e32 v68, 2, v150
	v_cmp_lt_i32_e32 vcc, v68, v67
	s_nop 1
	v_cndmask_b32_e32 v68, v150, v68, vcc
	v_lshlrev_b32_e32 v158, 2, v68
	ds_bpermute_b32 v68, v158, v66
	s_waitcnt lgkmcnt(0)
	v_add_f32_e32 v66, v66, v68
	v_xor_b32_e32 v68, 1, v150
	v_cmp_lt_i32_e32 vcc, v68, v67
	s_nop 1
	v_cndmask_b32_e32 v67, v150, v68, vcc
	v_lshlrev_b32_e32 v159, 2, v67
	ds_bpermute_b32 v67, v159, v66
	s_waitcnt lgkmcnt(0)
	v_add_f32_e32 v74, v66, v67
	v_fmamk_f32 v147, v74, 0xba000000, v147
	v_fmamk_f32 v145, v74, 0xba000000, v145
	v_fmamk_f32 v109, v74, 0xba000000, v109
	v_fmac_f32_e32 v146, 0xba000000, v74
	v_fmamk_f32 v143, v74, 0xba000000, v143
	v_fmac_f32_e32 v144, 0xba000000, v74
	v_mov_b32_e32 v68, v147
	v_mov_b32_e32 v69, v145
	v_fmac_f32_e32 v108, 0xba000000, v74
	v_fmac_f32_e32 v142, 0xba000000, v74
	v_mov_b32_e32 v66, v146
	v_mov_b32_e32 v67, v144
	v_pk_mul_f32 v[68:69], v[68:69], v[68:69]
	v_mov_b32_e32 v70, v109
	v_mov_b32_e32 v71, v143
	v_pk_fma_f32 v[66:67], v[66:67], v[66:67], v[68:69]
	v_mov_b32_e32 v68, v108
	v_mov_b32_e32 v69, v142
	v_pk_mul_f32 v[70:71], v[70:71], v[70:71]
	v_fmamk_f32 v137, v74, 0xba000000, v137
	v_pk_fma_f32 v[68:69], v[68:69], v[68:69], v[70:71]
	v_fmac_f32_e32 v136, 0xba000000, v74
	v_pk_add_f32 v[66:67], v[66:67], v[68:69]
	v_fmamk_f32 v139, v74, 0xba000000, v139
	v_fmac_f32_e32 v138, 0xba000000, v74
	v_pk_add_f32 v[66:67], v[66:67], v[66:67] op_sel_hi:[0,1]
	v_pk_mul_f32 v[68:69], v[138:139], v[138:139]
	v_pk_mul_f32 v[70:71], v[136:137], v[136:137]
	v_fmac_f32_e32 v132, 0xba000000, v74
	v_pk_mov_b32 v[72:73], v[70:71], v[68:69] op_sel:[1,0]
	v_mov_b32_e32 v71, v69
	v_fmamk_f32 v133, v74, 0xba000000, v133
	v_fmac_f32_e32 v130, 0xba000000, v74
	v_mul_f32_e32 v66, v132, v132
	v_pk_add_f32 v[68:69], v[72:73], v[70:71]
	v_fmamk_f32 v131, v74, 0xba000000, v131
	v_pk_fma_f32 v[70:71], v[132:133], v[132:133], v[66:67] op_sel_hi:[1,1,0]
	v_mul_f32_e32 v66, v130, v130
	v_pk_add_f32 v[68:69], v[68:69], v[68:69] op_sel_hi:[0,1]
	v_pk_fma_f32 v[72:73], v[130:131], v[130:131], v[66:67] op_sel_hi:[1,1,0]
	v_fmamk_f32 v125, v74, 0xba000000, v125
	v_fmac_f32_e32 v124, 0xba000000, v74
	v_fmamk_f32 v127, v74, 0xba000000, v127
	v_fmac_f32_e32 v126, 0xba000000, v74
	v_mul_f32_e32 v70, v126, v126
	v_mul_f32_e32 v72, v127, v127
	v_mul_f32_e32 v68, v124, v124
	v_mul_f32_e32 v66, v125, v125
	v_pk_add_f32 v[70:71], v[70:71], v[72:73]
	v_pk_add_f32 v[66:67], v[68:69], v[66:67]
	v_fmamk_f32 v119, v74, 0xba000000, v119
	v_pk_add_f32 v[66:67], v[70:71], v[66:67]
	v_fmac_f32_e32 v118, 0xba000000, v74
	v_fmamk_f32 v121, v74, 0xba000000, v121
	v_fmac_f32_e32 v120, 0xba000000, v74
	v_pk_add_f32 v[66:67], v[66:67], v[66:67] op_sel_hi:[0,1]
	v_pk_mul_f32 v[68:69], v[120:121], v[120:121]
	v_pk_mul_f32 v[70:71], v[118:119], v[118:119]
	v_fmac_f32_e32 v114, 0xba000000, v74
	v_pk_mov_b32 v[72:73], v[70:71], v[68:69] op_sel:[1,0]
	v_mov_b32_e32 v71, v69
	v_fmamk_f32 v115, v74, 0xba000000, v115
	v_fmac_f32_e32 v112, 0xba000000, v74
	v_mul_f32_e32 v66, v114, v114
	v_pk_add_f32 v[68:69], v[72:73], v[70:71]
	v_fmamk_f32 v113, v74, 0xba000000, v113
	v_pk_fma_f32 v[70:71], v[114:115], v[114:115], v[66:67] op_sel_hi:[1,1,0]
	v_mul_f32_e32 v66, v112, v112
	v_pk_add_f32 v[68:69], v[68:69], v[68:69] op_sel_hi:[0,1]
	v_pk_fma_f32 v[72:73], v[112:113], v[112:113], v[66:67] op_sel_hi:[1,1,0]
	v_fmamk_f32 v103, v74, 0xba000000, v103
	v_fmac_f32_e32 v102, 0xba000000, v74
	v_fmamk_f32 v105, v74, 0xba000000, v105
	v_fmac_f32_e32 v104, 0xba000000, v74
	v_mul_f32_e32 v70, v104, v104
	v_mul_f32_e32 v72, v105, v105
	v_mul_f32_e32 v68, v102, v102
	v_mul_f32_e32 v66, v103, v103
	v_pk_add_f32 v[70:71], v[70:71], v[72:73]
	v_pk_add_f32 v[66:67], v[68:69], v[66:67]
	s_nop 0
	v_pk_add_f32 v[66:67], v[70:71], v[66:67]
	ds_read_b128 v[70:73], v96
	ds_read_b128 v[74:77], v97
	v_add_f32_e32 v66, v66, v67
	ds_bpermute_b32 v67, v154, v66
	global_load_dwordx2 v[98:99], v[78:79], off nt
	s_waitcnt lgkmcnt(1)
	v_pk_add_f32 v[74:75], v[74:75], 1.0 op_sel_hi:[1,0]
	v_pk_add_f32 v[76:77], v[76:77], 1.0 op_sel_hi:[1,0]
	s_waitcnt lgkmcnt(0)
	v_add_f32_e32 v66, v66, v67
	ds_bpermute_b32 v67, v155, v66
	s_waitcnt lgkmcnt(0)
	v_add_f32_e32 v66, v66, v67
	ds_bpermute_b32 v67, v156, v66
	s_waitcnt lgkmcnt(0)
	v_add_f32_e32 v66, v66, v67
	ds_bpermute_b32 v67, v157, v66
	s_waitcnt lgkmcnt(0)
	v_add_f32_e32 v66, v66, v67
	ds_bpermute_b32 v67, v158, v66
	s_waitcnt lgkmcnt(0)
	v_add_f32_e32 v66, v66, v67
	ds_bpermute_b32 v67, v159, v66
	s_waitcnt lgkmcnt(0)
	v_add_f32_e32 v66, v66, v67
	v_fmamk_f32 v66, v66, 0x3a000000, v148
	v_mul_f32_e32 v67, 0x4b800000, v66
	v_cmp_gt_f32_e32 vcc, s28, v66
	s_nop 1
	v_cndmask_b32_e32 v66, v66, v67, vcc
	v_rsq_f32_e32 v66, v66
	s_nop 0
	v_mul_f32_e32 v67, 0x45800000, v66
	v_cndmask_b32_e32 v110, v66, v67, vcc
	v_pk_mul_f32 v[78:79], v[146:147], v[110:111] op_sel_hi:[1,0]
	v_pk_mul_f32 v[80:81], v[108:109], v[110:111] op_sel_hi:[1,0]
	v_pk_fma_f32 v[78:79], v[62:63], v[78:79], v[58:59]
	v_pk_fma_f32 v[80:81], v[64:65], v[80:81], v[60:61]
	v_pk_fma_f32 v[86:87], v[74:75], v[78:79], v[70:71]
	v_lshl_add_u64 v[66:67], v[94:95], 2, s[12:13]
	v_med3_f32 v70, v86, s29, v151
	v_med3_f32 v71, v87, s29, v151
	v_cvt_pk_fp8_f32 v90, v70, v71
	v_pk_fma_f32 v[88:89], v[76:77], v[80:81], v[72:73]
	global_load_dwordx4 v[66:69], v[66:67], off nt
	v_med3_f32 v70, v88, s29, v151
	v_med3_f32 v71, v89, s29, v151
	v_add_u32_e32 v108, s33, v82
	v_cvt_pk_fp8_f32 v90, v70, v71 op_sel:[0,0,1]
	ds_read_b128 v[70:73], v153
	v_add_u32_e32 v82, 0xfffff900, v108
	v_ashrrev_i32_e32 v83, 31, v82
	v_lshl_add_u64 v[84:85], v[82:83], 2, s[6:7]
	v_lshl_add_u64 v[74:75], s[4:5], 0, v[82:83]
	global_store_dwordx4 v[84:85], v[78:81], off nt
	global_store_dword v[74:75], v90, off
	ds_read_b128 v[74:77], v153 offset:8208
	s_waitcnt lgkmcnt(1)
	v_mul_f32_e32 v71, v71, v87
	v_fmac_f32_e32 v71, v70, v86
	v_mul_f32_e32 v70, v73, v89
	v_fmac_f32_e32 v70, v72, v88
	v_add_f32_e32 v70, v71, v70
	v_add_f32_e32 v95, 0, v70
	s_waitcnt lgkmcnt(0)
	v_mul_f32_e32 v75, v75, v87
	ds_read_b128 v[70:73], v153 offset:16416
	v_fmac_f32_e32 v75, v74, v86
	v_mul_f32_e32 v74, v77, v89
	v_fmac_f32_e32 v74, v76, v88
	v_add_f32_e32 v74, v75, v74
	v_add_f32_e32 v106, 0, v74
	ds_read_b128 v[74:77], v153 offset:24624
	s_waitcnt lgkmcnt(1)
	v_mul_f32_e32 v71, v71, v87
	v_fmac_f32_e32 v71, v70, v86
	v_mul_f32_e32 v70, v73, v89
	v_fmac_f32_e32 v70, v72, v88
	v_add_f32_e32 v70, v71, v70
	v_add_f32_e32 v107, 0, v70
	s_waitcnt lgkmcnt(0)
	v_mul_f32_e32 v75, v75, v87
	ds_read_b128 v[70:73], v153 offset:32832
	v_fmac_f32_e32 v75, v74, v86
	v_mul_f32_e32 v74, v77, v89
	v_fmac_f32_e32 v74, v76, v88
	v_add_f32_e32 v74, v75, v74
	v_add_f32_e32 v109, 0, v74
	ds_read_b128 v[74:77], v153 offset:41040
	s_waitcnt lgkmcnt(1)
	v_mul_f32_e32 v71, v71, v87
	v_fmac_f32_e32 v71, v70, v86
	v_mul_f32_e32 v70, v73, v89
	v_fmac_f32_e32 v70, v72, v88
	v_add_f32_e32 v70, v71, v70
	v_add_f32_e32 v116, 0, v70
	s_waitcnt lgkmcnt(0)
	v_mul_f32_e32 v75, v75, v87
	ds_read_b128 v[70:73], v153 offset:49248
	v_fmac_f32_e32 v75, v74, v86
	v_mul_f32_e32 v74, v77, v89
	v_fmac_f32_e32 v74, v76, v88
	v_add_f32_e32 v74, v75, v74
	v_add_f32_e32 v117, 0, v74
	ds_read_b128 v[74:77], v153 offset:57456
	s_waitcnt lgkmcnt(1)
	v_mul_f32_e32 v71, v71, v87
	v_fmac_f32_e32 v71, v70, v86
	v_mul_f32_e32 v70, v73, v89
	v_fmac_f32_e32 v70, v72, v88
	v_add_f32_e32 v70, v71, v70
	v_add_f32_e32 v122, 0, v70
	s_waitcnt lgkmcnt(0)
	v_mul_f32_e32 v75, v75, v87
	v_add_u32_e32 v70, 0x10080, v153
	v_fmac_f32_e32 v75, v74, v86
	v_mul_f32_e32 v74, v77, v89
	ds_read_b128 v[70:73], v70
	v_fmac_f32_e32 v74, v76, v88
	v_add_f32_e32 v74, v75, v74
	v_add_f32_e32 v123, 0, v74
	v_add_u32_e32 v74, 0x12090, v153
	ds_read_b128 v[74:77], v74
	s_waitcnt lgkmcnt(1)
	v_mul_f32_e32 v71, v71, v87
	v_fmac_f32_e32 v71, v70, v86
	v_mul_f32_e32 v70, v73, v89
	v_fmac_f32_e32 v70, v72, v88
	v_add_f32_e32 v70, v71, v70
	v_add_f32_e32 v128, 0, v70
	s_waitcnt lgkmcnt(0)
	v_mul_f32_e32 v75, v75, v87
	v_add_u32_e32 v70, 0x140a0, v153
	v_fmac_f32_e32 v75, v74, v86
	v_mul_f32_e32 v74, v77, v89
	ds_read_b128 v[70:73], v70
	v_fmac_f32_e32 v74, v76, v88
	v_add_f32_e32 v74, v75, v74
	v_add_f32_e32 v129, 0, v74
	v_add_u32_e32 v74, 0x160b0, v153
	ds_read_b128 v[74:77], v74
	s_waitcnt lgkmcnt(1)
	v_mul_f32_e32 v71, v71, v87
	v_fmac_f32_e32 v71, v70, v86
	v_mul_f32_e32 v70, v73, v89
	v_fmac_f32_e32 v70, v72, v88
	v_add_f32_e32 v70, v71, v70
	v_add_f32_e32 v134, 0, v70
	s_waitcnt lgkmcnt(0)
	v_mul_f32_e32 v75, v75, v87
	v_add_u32_e32 v70, 0x180c0, v153
	v_fmac_f32_e32 v75, v74, v86
	v_mul_f32_e32 v74, v77, v89
	ds_read_b128 v[70:73], v70
	v_fmac_f32_e32 v74, v76, v88
	v_add_f32_e32 v74, v75, v74
	v_add_f32_e32 v135, 0, v74
	v_add_u32_e32 v74, 0x1a0d0, v153
	ds_read_b128 v[74:77], v74
	s_waitcnt lgkmcnt(1)
	v_mul_f32_e32 v71, v71, v87
	v_fmac_f32_e32 v71, v70, v86
	v_mul_f32_e32 v70, v73, v89
	v_fmac_f32_e32 v70, v72, v88
	v_add_f32_e32 v70, v71, v70
	v_add_f32_e32 v140, 0, v70
	s_waitcnt lgkmcnt(0)
	v_mul_f32_e32 v75, v75, v87
	v_add_u32_e32 v70, 0x1c0e0, v153
	v_fmac_f32_e32 v75, v74, v86
	v_mul_f32_e32 v74, v77, v89
	ds_read_b128 v[70:73], v70
	v_fmac_f32_e32 v74, v76, v88
	v_add_f32_e32 v74, v75, v74
	v_add_f32_e32 v141, 0, v74
	v_add_u32_e32 v74, 0x1e0f0, v153
	ds_read_b128 v[74:77], v74
	s_waitcnt lgkmcnt(1)
	v_mul_f32_e32 v71, v71, v87
	v_fmac_f32_e32 v71, v70, v86
	v_mul_f32_e32 v70, v73, v89
	v_fmac_f32_e32 v70, v72, v88
	v_add_f32_e32 v70, v71, v70
	v_add_f32_e32 v146, 0, v70
	s_waitcnt lgkmcnt(0)
	v_mul_f32_e32 v70, v75, v87
	v_mul_f32_e32 v71, v77, v89
	v_fmac_f32_e32 v70, v74, v86
	v_fmac_f32_e32 v71, v76, v88
	v_add_f32_e32 v70, v70, v71
	v_add_f32_e32 v147, 0, v70
	ds_read_b128 v[74:77], v96 offset:1024
	ds_read_b128 v[78:81], v97 offset:1024
	v_add_u32_e32 v82, 0x100, v94
	v_ashrrev_i32_e32 v83, 31, v82
	v_lshl_add_u64 v[70:71], v[82:83], 2, s[12:13]
	v_lshl_add_u64 v[82:83], v[82:83], 1, s[10:11]
	global_load_dwordx2 v[100:101], v[82:83], off nt
	v_pk_mul_f32 v[82:83], v[144:145], v[110:111] op_sel_hi:[1,0]
	s_waitcnt lgkmcnt(0)
	v_pk_add_f32 v[78:79], v[78:79], 1.0 op_sel_hi:[1,0]
	v_pk_fma_f32 v[82:83], v[54:55], v[82:83], v[50:51]
	v_pk_mul_f32 v[84:85], v[142:143], v[110:111] op_sel_hi:[1,0]
	v_pk_fma_f32 v[90:91], v[78:79], v[82:83], v[74:75]
	v_mov_b32_e32 v142, 0
	v_med3_f32 v74, v90, s29, v151
	v_med3_f32 v75, v91, s29, v151
	v_cvt_pk_fp8_f32 v142, v74, v75
	v_pk_fma_f32 v[84:85], v[56:57], v[84:85], v[52:53]
	v_pk_add_f32 v[80:81], v[80:81], 1.0 op_sel_hi:[1,0]
	global_load_dwordx4 v[70:73], v[70:71], off nt
	v_pk_fma_f32 v[92:93], v[80:81], v[84:85], v[76:77]
	v_add_u32_e32 v86, 0xfffffa00, v108
	v_med3_f32 v74, v92, s29, v151
	v_med3_f32 v75, v93, s29, v151
	v_cvt_pk_fp8_f32 v142, v74, v75 op_sel:[0,0,1]
	ds_read_b128 v[74:77], v153 offset:1024
	v_ashrrev_i32_e32 v87, 31, v86
	v_lshl_add_u64 v[88:89], v[86:87], 2, s[6:7]
	v_lshl_add_u64 v[78:79], s[4:5], 0, v[86:87]
	global_store_dwordx4 v[88:89], v[82:85], off nt
	global_store_dword v[78:79], v142, off
	ds_read_b128 v[78:81], v153 offset:9232
	s_waitcnt lgkmcnt(1)
	v_mul_f32_e32 v75, v75, v91
	v_fmac_f32_e32 v75, v74, v90
	v_mul_f32_e32 v74, v77, v93
	v_fmac_f32_e32 v74, v76, v92
	v_add_f32_e32 v74, v75, v74
	v_add_f32_e32 v95, v74, v95
	s_waitcnt lgkmcnt(0)
	v_mul_f32_e32 v79, v79, v91
	ds_read_b128 v[74:77], v153 offset:17440
	v_fmac_f32_e32 v79, v78, v90
	v_mul_f32_e32 v78, v81, v93
	v_fmac_f32_e32 v78, v80, v92
	v_add_f32_e32 v78, v79, v78
	v_add_f32_e32 v142, v78, v106
	ds_read_b128 v[78:81], v153 offset:25648
	s_waitcnt lgkmcnt(1)
	v_mul_f32_e32 v75, v75, v91
	v_fmac_f32_e32 v75, v74, v90
	v_mul_f32_e32 v74, v77, v93
	v_fmac_f32_e32 v74, v76, v92
	v_add_f32_e32 v74, v75, v74
	v_add_f32_e32 v143, v74, v107
	s_waitcnt lgkmcnt(0)
	v_mul_f32_e32 v79, v79, v91
	ds_read_b128 v[74:77], v153 offset:33856
	v_fmac_f32_e32 v79, v78, v90
	v_mul_f32_e32 v78, v81, v93
	v_fmac_f32_e32 v78, v80, v92
	v_add_f32_e32 v78, v79, v78
	v_add_f32_e32 v109, v78, v109
	ds_read_b128 v[78:81], v153 offset:42064
	s_waitcnt lgkmcnt(1)
	v_mul_f32_e32 v75, v91, v75
	v_fmac_f32_e32 v75, v90, v74
	v_mul_f32_e32 v74, v93, v77
	v_fmac_f32_e32 v74, v92, v76
	v_add_f32_e32 v74, v75, v74
	v_add_f32_e32 v144, v74, v116
	s_waitcnt lgkmcnt(0)
	v_mul_f32_e32 v79, v91, v79
	ds_read_b128 v[74:77], v153 offset:50272
	v_fmac_f32_e32 v79, v90, v78
	v_mul_f32_e32 v78, v93, v81
	v_fmac_f32_e32 v78, v92, v80
	v_add_f32_e32 v78, v79, v78
	v_add_f32_e32 v145, v117, v78
	ds_read_b128 v[78:81], v153 offset:58480
	s_waitcnt lgkmcnt(1)
	v_mul_f32_e32 v75, v91, v75
	v_fmac_f32_e32 v75, v90, v74
	v_mul_f32_e32 v74, v93, v77
	v_fmac_f32_e32 v74, v92, v76
	v_add_f32_e32 v74, v75, v74
	v_add_f32_e32 v160, v122, v74
	s_waitcnt lgkmcnt(0)
	v_mul_f32_e32 v79, v91, v79
	v_add_u32_e32 v74, 0x10480, v153
	v_fmac_f32_e32 v79, v90, v78
	v_mul_f32_e32 v78, v93, v81
	ds_read_b128 v[74:77], v74
	v_fmac_f32_e32 v78, v92, v80
	v_add_f32_e32 v78, v79, v78
	v_add_f32_e32 v161, v123, v78
	v_add_u32_e32 v78, 0x12490, v153
	ds_read_b128 v[78:81], v78
	s_waitcnt lgkmcnt(1)
	v_mul_f32_e32 v75, v91, v75
	v_fmac_f32_e32 v75, v90, v74
	v_mul_f32_e32 v74, v93, v77
	v_fmac_f32_e32 v74, v92, v76
	v_add_f32_e32 v74, v75, v74
	v_add_f32_e32 v128, v128, v74
	s_waitcnt lgkmcnt(0)
	v_mul_f32_e32 v79, v91, v79
	v_add_u32_e32 v74, 0x144a0, v153
	v_fmac_f32_e32 v79, v90, v78
	v_mul_f32_e32 v78, v93, v81
	ds_read_b128 v[74:77], v74
	v_fmac_f32_e32 v78, v92, v80
	v_add_f32_e32 v78, v79, v78
	v_add_f32_e32 v129, v129, v78
	v_add_u32_e32 v78, 0x164b0, v153
	ds_read_b128 v[78:81], v78
	s_waitcnt lgkmcnt(1)
	v_mul_f32_e32 v75, v91, v75
	v_fmac_f32_e32 v75, v90, v74
	v_mul_f32_e32 v74, v93, v77
	v_fmac_f32_e32 v74, v92, v76
	v_add_f32_e32 v74, v75, v74
	v_add_f32_e32 v134, v134, v74
	s_waitcnt lgkmcnt(0)
	v_mul_f32_e32 v79, v91, v79
	v_add_u32_e32 v74, 0x184c0, v153
	v_fmac_f32_e32 v79, v90, v78
	v_mul_f32_e32 v78, v93, v81
	ds_read_b128 v[74:77], v74
	v_fmac_f32_e32 v78, v92, v80
	v_add_f32_e32 v78, v79, v78
	v_add_f32_e32 v135, v135, v78
	v_add_u32_e32 v78, 0x1a4d0, v153
	ds_read_b128 v[78:81], v78
	s_waitcnt lgkmcnt(1)
	v_mul_f32_e32 v75, v91, v75
	v_fmac_f32_e32 v75, v90, v74
	v_mul_f32_e32 v74, v93, v77
	v_fmac_f32_e32 v74, v92, v76
	v_add_f32_e32 v74, v75, v74
	v_add_f32_e32 v140, v140, v74
	s_waitcnt lgkmcnt(0)
	v_mul_f32_e32 v79, v91, v79
	v_add_u32_e32 v74, 0x1c4e0, v153
	v_fmac_f32_e32 v79, v90, v78
	v_mul_f32_e32 v78, v93, v81
	ds_read_b128 v[74:77], v74
	v_fmac_f32_e32 v78, v92, v80
	v_add_f32_e32 v78, v79, v78
	v_add_f32_e32 v141, v141, v78
	v_add_u32_e32 v78, 0x1e4f0, v153
	ds_read_b128 v[78:81], v78
	s_waitcnt lgkmcnt(1)
	v_mul_f32_e32 v75, v91, v75
	v_fmac_f32_e32 v75, v90, v74
	v_mul_f32_e32 v74, v93, v77
	v_fmac_f32_e32 v74, v92, v76
	v_add_f32_e32 v74, v75, v74
	v_add_f32_e32 v146, v146, v74
	s_waitcnt lgkmcnt(0)
	v_mul_f32_e32 v74, v91, v79
	v_mul_f32_e32 v75, v93, v81
	v_fmac_f32_e32 v74, v90, v78
	v_fmac_f32_e32 v75, v92, v80
	v_add_f32_e32 v74, v74, v75
	v_add_f32_e32 v147, v147, v74
	ds_read_b128 v[78:81], v96 offset:2048
	ds_read_b128 v[82:85], v97 offset:2048
	v_add_u32_e32 v86, 0x200, v94
	v_ashrrev_i32_e32 v87, 31, v86
	v_lshl_add_u64 v[74:75], v[86:87], 2, s[12:13]
	v_lshl_add_u64 v[86:87], v[86:87], 1, s[10:11]
	global_load_dwordx2 v[106:107], v[86:87], off nt
	v_pk_mul_f32 v[86:87], v[136:137], v[110:111] op_sel_hi:[1,0]
	s_waitcnt lgkmcnt(0)
	v_pk_add_f32 v[82:83], v[82:83], 1.0 op_sel_hi:[1,0]
	v_pk_fma_f32 v[86:87], v[46:47], v[86:87], v[42:43]
	v_mov_b32_e32 v136, 0
	v_pk_fma_f32 v[116:117], v[86:87], v[82:83], v[78:79]
	v_pk_mul_f32 v[88:89], v[138:139], v[110:111] op_sel_hi:[1,0]
	v_med3_f32 v78, v116, s29, v151
	v_med3_f32 v79, v117, s29, v151
	v_cvt_pk_fp8_f32 v136, v78, v79
	v_pk_fma_f32 v[88:89], v[48:49], v[88:89], v[44:45]
	v_pk_add_f32 v[84:85], v[84:85], 1.0 op_sel_hi:[1,0]
	global_load_dwordx4 v[74:77], v[74:75], off nt
	v_pk_fma_f32 v[122:123], v[88:89], v[84:85], v[80:81]
	v_add_u32_e32 v90, 0xfffffb00, v108
	v_med3_f32 v78, v122, s29, v151
	v_med3_f32 v79, v123, s29, v151
	v_cvt_pk_fp8_f32 v136, v78, v79 op_sel:[0,0,1]
	ds_read_b128 v[78:81], v153 offset:2048
	v_ashrrev_i32_e32 v91, 31, v90
	v_lshl_add_u64 v[92:93], v[90:91], 2, s[6:7]
	v_lshl_add_u64 v[82:83], s[4:5], 0, v[90:91]
	global_store_dwordx4 v[92:93], v[86:89], off nt
	global_store_dword v[82:83], v136, off
	ds_read_b128 v[82:85], v153 offset:10256
	s_waitcnt lgkmcnt(1)
	v_mul_f32_e32 v79, v117, v79
	v_fmac_f32_e32 v79, v116, v78
	v_mul_f32_e32 v78, v123, v81
	v_fmac_f32_e32 v78, v122, v80
	v_add_f32_e32 v78, v79, v78
	v_add_f32_e32 v95, v95, v78
	s_waitcnt lgkmcnt(0)
	v_mul_f32_e32 v83, v117, v83
	ds_read_b128 v[78:81], v153 offset:18464
	v_fmac_f32_e32 v83, v116, v82
	v_mul_f32_e32 v82, v123, v85
	v_fmac_f32_e32 v82, v122, v84
	v_add_f32_e32 v82, v83, v82
	v_add_f32_e32 v136, v142, v82
	ds_read_b128 v[82:85], v153 offset:26672
	s_waitcnt lgkmcnt(1)
	v_mul_f32_e32 v79, v117, v79
	v_fmac_f32_e32 v79, v116, v78
	v_mul_f32_e32 v78, v123, v81
	v_fmac_f32_e32 v78, v122, v80
	v_add_f32_e32 v78, v79, v78
	v_add_f32_e32 v137, v143, v78
	s_waitcnt lgkmcnt(0)
	v_mul_f32_e32 v83, v117, v83
	ds_read_b128 v[78:81], v153 offset:34880
	v_fmac_f32_e32 v83, v116, v82
	v_mul_f32_e32 v82, v123, v85
	v_fmac_f32_e32 v82, v122, v84
	v_add_f32_e32 v82, v83, v82
	v_add_f32_e32 v109, v109, v82
	ds_read_b128 v[82:85], v153 offset:43088
	s_waitcnt lgkmcnt(1)
	v_mul_f32_e32 v79, v117, v79
	v_fmac_f32_e32 v79, v116, v78
	v_mul_f32_e32 v78, v123, v81
	v_fmac_f32_e32 v78, v122, v80
	v_add_f32_e32 v78, v79, v78
	v_add_f32_e32 v138, v144, v78
	s_waitcnt lgkmcnt(0)
	v_mul_f32_e32 v83, v117, v83
	ds_read_b128 v[78:81], v153 offset:51296
	v_fmac_f32_e32 v83, v116, v82
	v_mul_f32_e32 v82, v123, v85
	v_fmac_f32_e32 v82, v122, v84
	v_add_f32_e32 v82, v83, v82
	v_add_f32_e32 v139, v145, v82
	ds_read_b128 v[82:85], v153 offset:59504
	s_waitcnt lgkmcnt(1)
	v_mul_f32_e32 v79, v117, v79
	v_fmac_f32_e32 v79, v116, v78
	v_mul_f32_e32 v78, v123, v81
	v_fmac_f32_e32 v78, v122, v80
	v_add_f32_e32 v78, v79, v78
	v_add_f32_e32 v142, v160, v78
	s_waitcnt lgkmcnt(0)
	v_mul_f32_e32 v83, v117, v83
	v_add_u32_e32 v78, 0x10880, v153
	v_fmac_f32_e32 v83, v116, v82
	v_mul_f32_e32 v82, v123, v85
	ds_read_b128 v[78:81], v78
	v_fmac_f32_e32 v82, v122, v84
	v_add_f32_e32 v82, v83, v82
	v_add_f32_e32 v143, v161, v82
	v_add_u32_e32 v82, 0x12890, v153
	ds_read_b128 v[82:85], v82
	s_waitcnt lgkmcnt(1)
	v_mul_f32_e32 v79, v117, v79
	v_fmac_f32_e32 v79, v116, v78
	v_mul_f32_e32 v78, v123, v81
	v_fmac_f32_e32 v78, v122, v80
	v_add_f32_e32 v78, v79, v78
	v_add_f32_e32 v144, v128, v78
	s_waitcnt lgkmcnt(0)
	v_mul_f32_e32 v83, v117, v83
	v_add_u32_e32 v78, 0x148a0, v153
	v_fmac_f32_e32 v83, v116, v82
	v_mul_f32_e32 v82, v123, v85
	ds_read_b128 v[78:81], v78
	v_fmac_f32_e32 v82, v122, v84
	v_add_f32_e32 v82, v83, v82
	v_add_f32_e32 v145, v129, v82
	v_add_u32_e32 v82, 0x168b0, v153
	ds_read_b128 v[82:85], v82
	s_waitcnt lgkmcnt(1)
	v_mul_f32_e32 v79, v117, v79
	v_fmac_f32_e32 v79, v116, v78
	v_mul_f32_e32 v78, v123, v81
	v_fmac_f32_e32 v78, v122, v80
	v_add_f32_e32 v78, v79, v78
	v_add_f32_e32 v134, v134, v78
	s_waitcnt lgkmcnt(0)
	v_mul_f32_e32 v83, v117, v83
	v_add_u32_e32 v78, 0x188c0, v153
	v_fmac_f32_e32 v83, v116, v82
	v_mul_f32_e32 v82, v123, v85
	ds_read_b128 v[78:81], v78
	v_fmac_f32_e32 v82, v122, v84
	v_add_f32_e32 v82, v83, v82
	v_add_f32_e32 v135, v135, v82
	v_add_u32_e32 v82, 0x1a8d0, v153
	ds_read_b128 v[82:85], v82
	s_waitcnt lgkmcnt(1)
	v_mul_f32_e32 v79, v117, v79
	v_fmac_f32_e32 v79, v116, v78
	v_mul_f32_e32 v78, v123, v81
	v_fmac_f32_e32 v78, v122, v80
	v_add_f32_e32 v78, v79, v78
	v_add_f32_e32 v140, v140, v78
	s_waitcnt lgkmcnt(0)
	v_mul_f32_e32 v83, v117, v83
	v_add_u32_e32 v78, 0x1c8e0, v153
	v_fmac_f32_e32 v83, v116, v82
	v_mul_f32_e32 v82, v123, v85
	ds_read_b128 v[78:81], v78
	v_fmac_f32_e32 v82, v122, v84
	v_add_f32_e32 v82, v83, v82
	v_add_f32_e32 v141, v141, v82
	v_add_u32_e32 v82, 0x1e8f0, v153
	ds_read_b128 v[82:85], v82
	s_waitcnt lgkmcnt(1)
	v_mul_f32_e32 v79, v117, v79
	v_fmac_f32_e32 v79, v116, v78
	v_mul_f32_e32 v78, v123, v81
	v_fmac_f32_e32 v78, v122, v80
	v_add_f32_e32 v78, v79, v78
	v_add_f32_e32 v146, v146, v78
	s_waitcnt lgkmcnt(0)
	v_mul_f32_e32 v78, v117, v83
	v_mul_f32_e32 v79, v123, v85
	v_fmac_f32_e32 v78, v116, v82
	v_fmac_f32_e32 v79, v122, v84
	v_add_f32_e32 v78, v78, v79
	v_add_f32_e32 v147, v147, v78
	ds_read_b128 v[82:85], v96 offset:3072
	ds_read_b128 v[86:89], v97 offset:3072
	v_add_u32_e32 v90, 0x300, v94
	v_ashrrev_i32_e32 v91, 31, v90
	v_lshl_add_u64 v[78:79], v[90:91], 2, s[12:13]
	v_lshl_add_u64 v[90:91], v[90:91], 1, s[10:11]
	global_load_dwordx2 v[116:117], v[90:91], off nt
	v_pk_mul_f32 v[90:91], v[132:133], v[110:111] op_sel_hi:[1,0]
	s_waitcnt lgkmcnt(0)
	v_pk_add_f32 v[86:87], v[86:87], 1.0 op_sel_hi:[1,0]
	v_pk_fma_f32 v[90:91], v[38:39], v[90:91], v[34:35]
	v_pk_mul_f32 v[92:93], v[130:131], v[110:111] op_sel_hi:[1,0]
	v_pk_fma_f32 v[130:131], v[90:91], v[86:87], v[82:83]
	v_mov_b32_e32 v160, 0
	v_med3_f32 v82, v130, s29, v151
	v_med3_f32 v83, v131, s29, v151
	v_cvt_pk_fp8_f32 v160, v82, v83
	v_pk_fma_f32 v[92:93], v[40:41], v[92:93], v[36:37]
	v_pk_add_f32 v[88:89], v[88:89], 1.0 op_sel_hi:[1,0]
	global_load_dwordx4 v[78:81], v[78:79], off nt
	v_pk_fma_f32 v[132:133], v[92:93], v[88:89], v[84:85]
	v_add_u32_e32 v122, 0xfffffc00, v108
	v_med3_f32 v82, v132, s29, v151
	v_med3_f32 v83, v133, s29, v151
	v_cvt_pk_fp8_f32 v160, v82, v83 op_sel:[0,0,1]
	ds_read_b128 v[82:85], v153 offset:3072
	v_ashrrev_i32_e32 v123, 31, v122
	v_lshl_add_u64 v[128:129], v[122:123], 2, s[6:7]
	v_lshl_add_u64 v[86:87], s[4:5], 0, v[122:123]
	global_store_dwordx4 v[128:129], v[90:93], off nt
	global_store_dword v[86:87], v160, off
	ds_read_b128 v[86:89], v153 offset:11280
	s_waitcnt lgkmcnt(1)
	v_mul_f32_e32 v83, v131, v83
	v_fmac_f32_e32 v83, v130, v82
	v_mul_f32_e32 v82, v133, v85
	v_fmac_f32_e32 v82, v132, v84
	v_add_f32_e32 v82, v83, v82
	v_add_f32_e32 v95, v95, v82
	s_waitcnt lgkmcnt(0)
	v_mul_f32_e32 v87, v131, v87
	ds_read_b128 v[82:85], v153 offset:19488
	v_fmac_f32_e32 v87, v130, v86
	v_mul_f32_e32 v86, v133, v89
	v_fmac_f32_e32 v86, v132, v88
	v_add_f32_e32 v86, v87, v86
	v_add_f32_e32 v136, v136, v86
	ds_read_b128 v[86:89], v153 offset:27696
	s_waitcnt lgkmcnt(1)
	v_mul_f32_e32 v83, v131, v83
	v_fmac_f32_e32 v83, v130, v82
	v_mul_f32_e32 v82, v133, v85
	v_fmac_f32_e32 v82, v132, v84
	v_add_f32_e32 v82, v83, v82
	v_add_f32_e32 v137, v137, v82
	s_waitcnt lgkmcnt(0)
	v_mul_f32_e32 v87, v131, v87
	ds_read_b128 v[82:85], v153 offset:35904
	v_fmac_f32_e32 v87, v130, v86
	v_mul_f32_e32 v86, v133, v89
	v_fmac_f32_e32 v86, v132, v88
	v_add_f32_e32 v86, v87, v86
	v_add_f32_e32 v109, v109, v86
	ds_read_b128 v[86:89], v153 offset:44112
	s_waitcnt lgkmcnt(1)
	v_mul_f32_e32 v83, v131, v83
	v_fmac_f32_e32 v83, v130, v82
	v_mul_f32_e32 v82, v133, v85
	v_fmac_f32_e32 v82, v132, v84
	v_add_f32_e32 v82, v83, v82
	v_add_f32_e32 v138, v138, v82
	s_waitcnt lgkmcnt(0)
	v_mul_f32_e32 v87, v131, v87
	ds_read_b128 v[82:85], v153 offset:52320
	v_fmac_f32_e32 v87, v130, v86
	v_mul_f32_e32 v86, v133, v89
	v_fmac_f32_e32 v86, v132, v88
	v_add_f32_e32 v86, v87, v86
	v_add_f32_e32 v139, v139, v86
	ds_read_b128 v[86:89], v153 offset:60528
	s_waitcnt lgkmcnt(1)
	v_mul_f32_e32 v83, v131, v83
	v_fmac_f32_e32 v83, v130, v82
	v_mul_f32_e32 v82, v133, v85
	v_fmac_f32_e32 v82, v132, v84
	v_add_f32_e32 v82, v83, v82
	v_add_f32_e32 v142, v142, v82
	s_waitcnt lgkmcnt(0)
	v_mul_f32_e32 v87, v131, v87
	v_add_u32_e32 v82, 0x10c80, v153
	v_fmac_f32_e32 v87, v130, v86
	v_mul_f32_e32 v86, v133, v89
	ds_read_b128 v[82:85], v82
	v_fmac_f32_e32 v86, v132, v88
	v_add_f32_e32 v86, v87, v86
	v_add_f32_e32 v143, v143, v86
	v_add_u32_e32 v86, 0x12c90, v153
	ds_read_b128 v[86:89], v86
	s_waitcnt lgkmcnt(1)
	v_mul_f32_e32 v83, v131, v83
	v_fmac_f32_e32 v83, v130, v82
	v_mul_f32_e32 v82, v133, v85
	v_fmac_f32_e32 v82, v132, v84
	v_add_f32_e32 v82, v83, v82
	v_add_f32_e32 v144, v144, v82
	s_waitcnt lgkmcnt(0)
	v_mul_f32_e32 v87, v131, v87
	v_add_u32_e32 v82, 0x14ca0, v153
	v_fmac_f32_e32 v87, v130, v86
	v_mul_f32_e32 v86, v133, v89
	ds_read_b128 v[82:85], v82
	v_fmac_f32_e32 v86, v132, v88
	v_add_f32_e32 v86, v87, v86
	v_add_f32_e32 v145, v145, v86
	v_add_u32_e32 v86, 0x16cb0, v153
	ds_read_b128 v[86:89], v86
	s_waitcnt lgkmcnt(1)
	v_mul_f32_e32 v83, v131, v83
	v_fmac_f32_e32 v83, v130, v82
	v_mul_f32_e32 v82, v133, v85
	v_fmac_f32_e32 v82, v132, v84
	v_add_f32_e32 v82, v83, v82
	v_add_f32_e32 v160, v134, v82
	s_waitcnt lgkmcnt(0)
	v_mul_f32_e32 v87, v131, v87
	v_add_u32_e32 v82, 0x18cc0, v153
	v_fmac_f32_e32 v87, v130, v86
	v_mul_f32_e32 v86, v133, v89
	ds_read_b128 v[82:85], v82
	v_fmac_f32_e32 v86, v132, v88
	v_add_f32_e32 v86, v87, v86
	v_add_f32_e32 v161, v135, v86
	v_add_u32_e32 v86, 0x1acd0, v153
	ds_read_b128 v[86:89], v86
	s_waitcnt lgkmcnt(1)
	v_mul_f32_e32 v83, v131, v83
	v_fmac_f32_e32 v83, v130, v82
	v_mul_f32_e32 v82, v133, v85
	v_fmac_f32_e32 v82, v132, v84
	v_add_f32_e32 v82, v83, v82
	v_add_f32_e32 v140, v140, v82
	s_waitcnt lgkmcnt(0)
	v_mul_f32_e32 v87, v131, v87
	v_add_u32_e32 v82, 0x1cce0, v153
	v_fmac_f32_e32 v87, v130, v86
	v_mul_f32_e32 v86, v133, v89
	ds_read_b128 v[82:85], v82
	v_fmac_f32_e32 v86, v132, v88
	v_add_f32_e32 v86, v87, v86
	v_add_f32_e32 v141, v141, v86
	v_add_u32_e32 v86, 0x1ecf0, v153
	ds_read_b128 v[86:89], v86
	s_waitcnt lgkmcnt(1)
	v_mul_f32_e32 v83, v131, v83
	v_fmac_f32_e32 v83, v130, v82
	v_mul_f32_e32 v82, v133, v85
	v_fmac_f32_e32 v82, v132, v84
	v_add_f32_e32 v82, v83, v82
	v_add_f32_e32 v146, v146, v82
	s_waitcnt lgkmcnt(0)
	v_mul_f32_e32 v82, v131, v87
	v_mul_f32_e32 v83, v133, v89
	v_fmac_f32_e32 v82, v130, v86
	v_fmac_f32_e32 v83, v132, v88
	v_add_f32_e32 v82, v82, v83
	v_add_f32_e32 v147, v147, v82
	ds_read_b128 v[86:89], v96 offset:4096
	ds_read_b128 v[90:93], v97 offset:4096
	v_pk_mul_f32 v[128:129], v[126:127], v[110:111] op_sel_hi:[1,0]
	v_pk_mul_f32 v[124:125], v[124:125], v[110:111] op_sel_hi:[1,0]
	v_mov_b32_e32 v162, 0
	v_pk_fma_f32 v[126:127], v[32:33], v[124:125], v[28:29]
	v_pk_fma_f32 v[124:125], v[30:31], v[128:129], v[26:27]
	s_waitcnt lgkmcnt(0)
	v_pk_add_f32 v[90:91], v[90:91], 1.0 op_sel_hi:[1,0]
	v_add_u32_e32 v122, 0x400, v94
	v_pk_fma_f32 v[132:133], v[124:125], v[90:91], v[86:87]
	v_pk_add_f32 v[92:93], v[92:93], 1.0 op_sel_hi:[1,0]
	v_med3_f32 v86, v132, s29, v151
	v_med3_f32 v87, v133, s29, v151
	v_cvt_pk_fp8_f32 v162, v86, v87
	v_ashrrev_i32_e32 v123, 31, v122
	v_pk_fma_f32 v[134:135], v[126:127], v[92:93], v[88:89]
	v_lshl_add_u64 v[82:83], v[122:123], 2, s[12:13]
	v_lshl_add_u64 v[122:123], v[122:123], 1, s[10:11]
	v_med3_f32 v86, v134, s29, v151
	v_med3_f32 v87, v135, s29, v151
	global_load_dwordx4 v[82:85], v[82:83], off nt
	v_cvt_pk_fp8_f32 v162, v86, v87 op_sel:[0,0,1]
	global_load_dwordx2 v[122:123], v[122:123], off nt
	ds_read_b128 v[86:89], v153 offset:4096
	v_add_u32_e32 v128, 0xfffffd00, v108
	v_ashrrev_i32_e32 v129, 31, v128
	v_lshl_add_u64 v[130:131], v[128:129], 2, s[6:7]
	v_lshl_add_u64 v[90:91], s[4:5], 0, v[128:129]
	global_store_dwordx4 v[130:131], v[124:127], off nt
	global_store_dword v[90:91], v162, off
	ds_read_b128 v[90:93], v153 offset:12304
	s_waitcnt lgkmcnt(1)
	v_mul_f32_e32 v87, v133, v87
	v_fmac_f32_e32 v87, v132, v86
	v_mul_f32_e32 v86, v135, v89
	v_fmac_f32_e32 v86, v134, v88
	v_add_f32_e32 v86, v87, v86
	v_add_f32_e32 v95, v95, v86
	s_waitcnt lgkmcnt(0)
	v_mul_f32_e32 v91, v133, v91
	ds_read_b128 v[86:89], v153 offset:20512
	v_fmac_f32_e32 v91, v132, v90
	v_mul_f32_e32 v90, v135, v93
	v_fmac_f32_e32 v90, v134, v92
	v_add_f32_e32 v90, v91, v90
	v_add_f32_e32 v136, v136, v90
	ds_read_b128 v[90:93], v153 offset:28720
	s_waitcnt lgkmcnt(1)
	v_mul_f32_e32 v87, v133, v87
	v_fmac_f32_e32 v87, v132, v86
	v_mul_f32_e32 v86, v135, v89
	v_fmac_f32_e32 v86, v134, v88
	v_add_f32_e32 v86, v87, v86
	v_add_f32_e32 v137, v137, v86
	s_waitcnt lgkmcnt(0)
	v_mul_f32_e32 v91, v133, v91
	ds_read_b128 v[86:89], v153 offset:36928
	v_fmac_f32_e32 v91, v132, v90
	v_mul_f32_e32 v90, v135, v93
	v_fmac_f32_e32 v90, v134, v92
	v_add_f32_e32 v90, v91, v90
	v_add_f32_e32 v109, v109, v90
	ds_read_b128 v[90:93], v153 offset:45136
	s_waitcnt lgkmcnt(1)
	v_mul_f32_e32 v87, v133, v87
	v_fmac_f32_e32 v87, v132, v86
	v_mul_f32_e32 v86, v135, v89
	v_fmac_f32_e32 v86, v134, v88
	v_add_f32_e32 v86, v87, v86
	v_add_f32_e32 v138, v138, v86
	s_waitcnt lgkmcnt(0)
	v_mul_f32_e32 v91, v133, v91
	ds_read_b128 v[86:89], v153 offset:53344
	v_fmac_f32_e32 v91, v132, v90
	v_mul_f32_e32 v90, v135, v93
	v_fmac_f32_e32 v90, v134, v92
	v_add_f32_e32 v90, v91, v90
	v_add_f32_e32 v139, v139, v90
	ds_read_b128 v[90:93], v153 offset:61552
	s_waitcnt lgkmcnt(1)
	v_mul_f32_e32 v87, v133, v87
	v_fmac_f32_e32 v87, v132, v86
	v_mul_f32_e32 v86, v135, v89
	v_fmac_f32_e32 v86, v134, v88
	v_add_f32_e32 v86, v87, v86
	v_add_f32_e32 v142, v142, v86
	s_waitcnt lgkmcnt(0)
	v_mul_f32_e32 v91, v133, v91
	v_add_u32_e32 v86, 0x11080, v153
	v_fmac_f32_e32 v91, v132, v90
	v_mul_f32_e32 v90, v135, v93
	ds_read_b128 v[86:89], v86
	v_fmac_f32_e32 v90, v134, v92
	v_add_f32_e32 v90, v91, v90
	v_add_f32_e32 v143, v143, v90
	v_add_u32_e32 v90, 0x13090, v153
	ds_read_b128 v[90:93], v90
	s_waitcnt lgkmcnt(1)
	v_mul_f32_e32 v87, v133, v87
	v_fmac_f32_e32 v87, v132, v86
	v_mul_f32_e32 v86, v135, v89
	v_fmac_f32_e32 v86, v134, v88
	v_add_f32_e32 v86, v87, v86
	v_add_f32_e32 v144, v144, v86
	s_waitcnt lgkmcnt(0)
	v_mul_f32_e32 v91, v133, v91
	v_add_u32_e32 v86, 0x150a0, v153
	v_fmac_f32_e32 v91, v132, v90
	v_mul_f32_e32 v90, v135, v93
	ds_read_b128 v[86:89], v86
	v_fmac_f32_e32 v90, v134, v92
	v_add_f32_e32 v90, v91, v90
	v_add_f32_e32 v145, v145, v90
	v_add_u32_e32 v90, 0x170b0, v153
	ds_read_b128 v[90:93], v90
	s_waitcnt lgkmcnt(1)
	v_mul_f32_e32 v87, v133, v87
	v_fmac_f32_e32 v87, v132, v86
	v_mul_f32_e32 v86, v135, v89
	v_fmac_f32_e32 v86, v134, v88
	v_add_f32_e32 v86, v87, v86
	v_add_f32_e32 v160, v160, v86
	s_waitcnt lgkmcnt(0)
	v_mul_f32_e32 v91, v133, v91
	v_add_u32_e32 v86, 0x190c0, v153
	v_fmac_f32_e32 v91, v132, v90
	v_mul_f32_e32 v90, v135, v93
	ds_read_b128 v[86:89], v86
	v_fmac_f32_e32 v90, v134, v92
	v_add_f32_e32 v90, v91, v90
	v_add_f32_e32 v161, v161, v90
	v_add_u32_e32 v90, 0x1b0d0, v153
	ds_read_b128 v[90:93], v90
	s_waitcnt lgkmcnt(1)
	v_mul_f32_e32 v87, v133, v87
	v_fmac_f32_e32 v87, v132, v86
	v_mul_f32_e32 v86, v135, v89
	v_fmac_f32_e32 v86, v134, v88
	v_add_f32_e32 v86, v87, v86
	v_add_f32_e32 v140, v140, v86
	s_waitcnt lgkmcnt(0)
	v_mul_f32_e32 v91, v133, v91
	v_add_u32_e32 v86, 0x1d0e0, v153
	v_fmac_f32_e32 v91, v132, v90
	v_mul_f32_e32 v90, v135, v93
	ds_read_b128 v[86:89], v86
	v_fmac_f32_e32 v90, v134, v92
	v_add_f32_e32 v90, v91, v90
	v_add_f32_e32 v141, v141, v90
	v_add_u32_e32 v90, 0x1f0f0, v153
	ds_read_b128 v[90:93], v90
	s_waitcnt lgkmcnt(1)
	v_mul_f32_e32 v87, v133, v87
	v_fmac_f32_e32 v87, v132, v86
	v_mul_f32_e32 v86, v135, v89
	v_fmac_f32_e32 v86, v134, v88
	v_add_f32_e32 v86, v87, v86
	v_add_f32_e32 v146, v146, v86
	s_waitcnt lgkmcnt(0)
	v_mul_f32_e32 v86, v133, v91
	v_mul_f32_e32 v87, v135, v93
	v_fmac_f32_e32 v86, v132, v90
	v_fmac_f32_e32 v87, v134, v92
	v_add_f32_e32 v86, v86, v87
	v_add_f32_e32 v134, v147, v86
	ds_read_b128 v[90:93], v96 offset:5120
	ds_read_b128 v[124:127], v97 offset:5120
	v_pk_mul_f32 v[118:119], v[118:119], v[110:111] op_sel_hi:[1,0]
	v_mov_b32_e32 v135, 0
	v_pk_fma_f32 v[118:119], v[22:23], v[118:119], v[18:19]
	v_add_u32_e32 v128, 0x500, v94
	s_waitcnt lgkmcnt(0)
	v_pk_add_f32 v[124:125], v[124:125], 1.0 op_sel_hi:[1,0]
	v_pk_mul_f32 v[120:121], v[120:121], v[110:111] op_sel_hi:[1,0]
	v_pk_fma_f32 v[124:125], v[118:119], v[124:125], v[90:91]
	v_ashrrev_i32_e32 v129, 31, v128
	v_med3_f32 v90, v124, s29, v151
	v_med3_f32 v91, v125, s29, v151
	v_cvt_pk_fp8_f32 v135, v90, v91
	v_pk_fma_f32 v[120:121], v[24:25], v[120:121], v[20:21]
	v_pk_add_f32 v[126:127], v[126:127], 1.0 op_sel_hi:[1,0]
	v_lshl_add_u64 v[86:87], v[128:129], 2, s[12:13]
	v_lshl_add_u64 v[128:129], v[128:129], 1, s[10:11]
	v_pk_fma_f32 v[126:127], v[120:121], v[126:127], v[92:93]
	global_load_dwordx4 v[86:89], v[86:87], off nt
	v_med3_f32 v90, v126, s29, v151
	global_load_dwordx2 v[128:129], v[128:129], off nt
	v_med3_f32 v91, v127, s29, v151
	v_add_u32_e32 v130, 0xfffffe00, v108
	v_cvt_pk_fp8_f32 v135, v90, v91 op_sel:[0,0,1]
	ds_read_b128 v[90:93], v153 offset:5120
	v_ashrrev_i32_e32 v131, 31, v130
	v_lshl_add_u64 v[132:133], v[130:131], 2, s[6:7]
	global_store_dwordx4 v[132:133], v[118:121], off nt
	s_nop 1
	v_lshl_add_u64 v[118:119], s[4:5], 0, v[130:131]
	global_store_dword v[118:119], v135, off
	ds_read_b128 v[118:121], v153 offset:13328
	s_waitcnt lgkmcnt(1)
	v_mul_f32_e32 v91, v125, v91
	v_fmac_f32_e32 v91, v124, v90
	v_mul_f32_e32 v90, v127, v93
	v_fmac_f32_e32 v90, v126, v92
	v_add_f32_e32 v90, v91, v90
	v_add_f32_e32 v95, v95, v90
	s_waitcnt lgkmcnt(0)
	v_mul_f32_e32 v119, v125, v119
	ds_read_b128 v[90:93], v153 offset:21536
	v_fmac_f32_e32 v119, v124, v118
	v_mul_f32_e32 v118, v127, v121
	v_fmac_f32_e32 v118, v126, v120
	v_add_f32_e32 v118, v119, v118
	v_add_f32_e32 v136, v136, v118
	ds_read_b128 v[118:121], v153 offset:29744
	s_waitcnt lgkmcnt(1)
	v_mul_f32_e32 v91, v125, v91
	v_fmac_f32_e32 v91, v124, v90
	v_mul_f32_e32 v90, v127, v93
	v_fmac_f32_e32 v90, v126, v92
	v_add_f32_e32 v90, v91, v90
	v_add_f32_e32 v137, v137, v90
	s_waitcnt lgkmcnt(0)
	v_mul_f32_e32 v119, v125, v119
	ds_read_b128 v[90:93], v153 offset:37952
	v_fmac_f32_e32 v119, v124, v118
	v_mul_f32_e32 v118, v127, v121
	v_fmac_f32_e32 v118, v126, v120
	v_add_f32_e32 v118, v119, v118
	v_add_f32_e32 v109, v109, v118
	ds_read_b128 v[118:121], v153 offset:46160
	s_waitcnt lgkmcnt(1)
	v_mul_f32_e32 v91, v125, v91
	v_fmac_f32_e32 v91, v124, v90
	v_mul_f32_e32 v90, v127, v93
	v_fmac_f32_e32 v90, v126, v92
	v_add_f32_e32 v90, v91, v90
	v_add_f32_e32 v138, v138, v90
	s_waitcnt lgkmcnt(0)
	v_mul_f32_e32 v119, v125, v119
	ds_read_b128 v[90:93], v153 offset:54368
	v_fmac_f32_e32 v119, v124, v118
	v_mul_f32_e32 v118, v127, v121
	v_fmac_f32_e32 v118, v126, v120
	v_add_f32_e32 v118, v119, v118
	v_add_f32_e32 v139, v139, v118
	ds_read_b128 v[118:121], v153 offset:62576
	s_waitcnt lgkmcnt(1)
	v_mul_f32_e32 v91, v125, v91
	v_fmac_f32_e32 v91, v124, v90
	v_mul_f32_e32 v90, v127, v93
	v_fmac_f32_e32 v90, v126, v92
	v_add_f32_e32 v90, v91, v90
	v_add_f32_e32 v142, v142, v90
	s_waitcnt lgkmcnt(0)
	v_mul_f32_e32 v119, v125, v119
	v_add_u32_e32 v90, 0x11480, v153
	v_fmac_f32_e32 v119, v124, v118
	v_mul_f32_e32 v118, v127, v121
	ds_read_b128 v[90:93], v90
	v_fmac_f32_e32 v118, v126, v120
	v_add_f32_e32 v118, v119, v118
	v_add_f32_e32 v143, v143, v118
	v_add_u32_e32 v118, 0x13490, v153
	ds_read_b128 v[118:121], v118
	s_waitcnt lgkmcnt(1)
	v_mul_f32_e32 v91, v125, v91
	v_fmac_f32_e32 v91, v124, v90
	v_mul_f32_e32 v90, v127, v93
	v_fmac_f32_e32 v90, v126, v92
	v_add_f32_e32 v90, v91, v90
	v_add_f32_e32 v144, v144, v90
	s_waitcnt lgkmcnt(0)
	v_mul_f32_e32 v119, v125, v119
	v_add_u32_e32 v90, 0x154a0, v153
	v_fmac_f32_e32 v119, v124, v118
	v_mul_f32_e32 v118, v127, v121
	ds_read_b128 v[90:93], v90
	v_fmac_f32_e32 v118, v126, v120
	v_add_f32_e32 v118, v119, v118
	v_add_f32_e32 v145, v145, v118
	v_add_u32_e32 v118, 0x174b0, v153
	ds_read_b128 v[118:121], v118
	s_waitcnt lgkmcnt(1)
	v_mul_f32_e32 v91, v125, v91
	v_fmac_f32_e32 v91, v124, v90
	v_mul_f32_e32 v90, v127, v93
	v_fmac_f32_e32 v90, v126, v92
	v_add_f32_e32 v90, v91, v90
	v_add_f32_e32 v147, v160, v90
	s_waitcnt lgkmcnt(0)
	v_mul_f32_e32 v119, v125, v119
	v_add_u32_e32 v90, 0x194c0, v153
	v_fmac_f32_e32 v119, v124, v118
	v_mul_f32_e32 v118, v127, v121
	ds_read_b128 v[90:93], v90
	v_fmac_f32_e32 v118, v126, v120
	v_add_f32_e32 v118, v119, v118
	v_add_f32_e32 v160, v161, v118
	v_add_u32_e32 v118, 0x1b4d0, v153
	ds_read_b128 v[118:121], v118
	s_waitcnt lgkmcnt(1)
	v_mul_f32_e32 v91, v125, v91
	v_fmac_f32_e32 v91, v124, v90
	v_mul_f32_e32 v90, v127, v93
	v_fmac_f32_e32 v90, v126, v92
	v_add_f32_e32 v90, v91, v90
	v_add_f32_e32 v140, v140, v90
	s_waitcnt lgkmcnt(0)
	v_mul_f32_e32 v119, v125, v119
	v_add_u32_e32 v90, 0x1d4e0, v153
	v_fmac_f32_e32 v119, v124, v118
	v_mul_f32_e32 v118, v127, v121
	ds_read_b128 v[90:93], v90
	v_fmac_f32_e32 v118, v126, v120
	v_add_f32_e32 v118, v119, v118
	v_add_f32_e32 v141, v141, v118
	v_add_u32_e32 v118, 0x1f4f0, v153
	ds_read_b128 v[118:121], v118
	s_waitcnt lgkmcnt(1)
	v_mul_f32_e32 v91, v125, v91
	v_fmac_f32_e32 v91, v124, v90
	v_mul_f32_e32 v90, v127, v93
	v_fmac_f32_e32 v90, v126, v92
	v_add_f32_e32 v90, v91, v90
	v_add_f32_e32 v146, v146, v90
	s_waitcnt lgkmcnt(0)
	v_mul_f32_e32 v90, v125, v119
	v_mul_f32_e32 v91, v127, v121
	v_fmac_f32_e32 v90, v124, v118
	v_fmac_f32_e32 v91, v126, v120
	v_add_f32_e32 v90, v90, v91
	v_add_f32_e32 v161, v134, v90
	ds_read_b128 v[118:121], v96 offset:6144
	ds_read_b128 v[124:127], v97 offset:6144
	v_add_u32_e32 v130, 0x600, v94
	v_ashrrev_i32_e32 v131, 31, v130
	v_lshl_add_u64 v[90:91], v[130:131], 2, s[12:13]
	v_lshl_add_u64 v[130:131], v[130:131], 1, s[10:11]
	global_load_dwordx4 v[90:93], v[90:91], off nt
	v_pk_mul_f32 v[112:113], v[112:113], v[110:111] op_sel_hi:[1,0]
	global_load_dwordx2 v[134:135], v[130:131], off nt
	v_pk_mul_f32 v[130:131], v[114:115], v[110:111] op_sel_hi:[1,0]
	v_pk_fma_f32 v[114:115], v[16:17], v[112:113], v[12:13]
	v_pk_fma_f32 v[112:113], v[14:15], v[130:131], v[10:11]
	s_waitcnt lgkmcnt(0)
	v_pk_add_f32 v[124:125], v[124:125], 1.0 op_sel_hi:[1,0]
	v_mov_b32_e32 v162, 0
	v_pk_fma_f32 v[124:125], v[112:113], v[124:125], v[118:119]
	v_pk_add_f32 v[126:127], v[126:127], 1.0 op_sel_hi:[1,0]
	v_med3_f32 v118, v124, s29, v151
	v_med3_f32 v119, v125, s29, v151
	v_cvt_pk_fp8_f32 v162, v118, v119
	v_pk_fma_f32 v[126:127], v[114:115], v[126:127], v[120:121]
	v_add_u32_e32 v130, 0xffffff00, v108
	v_med3_f32 v118, v126, s29, v151
	v_med3_f32 v119, v127, s29, v151
	v_cvt_pk_fp8_f32 v162, v118, v119 op_sel:[0,0,1]
	ds_read_b128 v[118:121], v153 offset:6144
	v_ashrrev_i32_e32 v131, 31, v130
	v_lshl_add_u64 v[132:133], v[130:131], 2, s[6:7]
	global_store_dwordx4 v[132:133], v[112:115], off nt
	s_nop 1
	v_lshl_add_u64 v[112:113], s[4:5], 0, v[130:131]
	global_store_dword v[112:113], v162, off
	ds_read_b128 v[112:115], v153 offset:14352
	s_waitcnt lgkmcnt(1)
	v_mul_f32_e32 v119, v125, v119
	v_fmac_f32_e32 v119, v124, v118
	v_mul_f32_e32 v118, v127, v121
	v_fmac_f32_e32 v118, v126, v120
	v_add_f32_e32 v118, v119, v118
	v_add_f32_e32 v130, v95, v118
	ds_read_b128 v[118:121], v153 offset:22560
	s_waitcnt lgkmcnt(1)
	v_mul_f32_e32 v95, v125, v113
	v_fmac_f32_e32 v95, v124, v112
	v_mul_f32_e32 v112, v127, v115
	v_fmac_f32_e32 v112, v126, v114
	v_add_f32_e32 v95, v95, v112
	ds_read_b128 v[112:115], v153 offset:30768
	v_add_f32_e32 v131, v136, v95
	s_waitcnt lgkmcnt(1)
	v_mul_f32_e32 v95, v125, v119
	v_fmac_f32_e32 v95, v124, v118
	v_mul_f32_e32 v118, v127, v121
	v_fmac_f32_e32 v118, v126, v120
	v_add_f32_e32 v95, v95, v118
	v_add_f32_e32 v132, v137, v95
	s_waitcnt lgkmcnt(0)
	v_mul_f32_e32 v95, v125, v113
	ds_read_b128 v[118:121], v153 offset:38976
	v_fmac_f32_e32 v95, v124, v112
	v_mul_f32_e32 v112, v127, v115
	v_fmac_f32_e32 v112, v126, v114
	v_add_f32_e32 v95, v95, v112
	ds_read_b128 v[112:115], v153 offset:47184
	v_add_f32_e32 v133, v109, v95
	s_waitcnt lgkmcnt(1)
	v_mul_f32_e32 v95, v125, v119
	v_mul_f32_e32 v109, v127, v121
	v_fmac_f32_e32 v95, v124, v118
	v_fmac_f32_e32 v109, v126, v120
	ds_read_b128 v[118:121], v153 offset:55392
	v_add_f32_e32 v95, v95, v109
	v_add_f32_e32 v136, v138, v95
	s_waitcnt lgkmcnt(1)
	v_mul_f32_e32 v95, v125, v113
	v_mul_f32_e32 v109, v127, v115
	v_fmac_f32_e32 v95, v124, v112
	v_fmac_f32_e32 v109, v126, v114
	ds_read_b128 v[112:115], v153 offset:63600
	v_add_f32_e32 v95, v95, v109
	v_add_f32_e32 v137, v139, v95
	s_waitcnt lgkmcnt(1)
	v_mul_f32_e32 v95, v125, v119
	v_mul_f32_e32 v109, v127, v121
	v_fmac_f32_e32 v95, v124, v118
	v_fmac_f32_e32 v109, v126, v120
	v_add_f32_e32 v95, v95, v109
	v_add_f32_e32 v138, v142, v95
	s_waitcnt lgkmcnt(0)
	v_mul_f32_e32 v95, v125, v113
	v_fmac_f32_e32 v95, v124, v112
	v_mul_f32_e32 v109, v127, v115
	v_add_u32_e32 v112, 0x11880, v153
	v_fmac_f32_e32 v109, v126, v114
	ds_read_b128 v[112:115], v112
	v_add_f32_e32 v95, v95, v109
	v_add_f32_e32 v139, v143, v95
	v_add_u32_e32 v95, 0x13890, v153
	ds_read_b128 v[118:121], v95
	s_waitcnt lgkmcnt(1)
	v_mul_f32_e32 v95, v125, v113
	v_mul_f32_e32 v109, v127, v115
	v_fmac_f32_e32 v95, v124, v112
	v_fmac_f32_e32 v109, v126, v114
	v_add_f32_e32 v95, v95, v109
	v_add_f32_e32 v142, v144, v95
	s_waitcnt lgkmcnt(0)
	v_mul_f32_e32 v95, v125, v119
	v_mul_f32_e32 v109, v127, v121
	v_add_u32_e32 v112, 0x158a0, v153
	v_fmac_f32_e32 v95, v124, v118
	v_fmac_f32_e32 v109, v126, v120
	ds_read_b128 v[112:115], v112
	v_add_f32_e32 v95, v95, v109
	v_add_f32_e32 v143, v145, v95
	v_add_u32_e32 v95, 0x178b0, v153
	ds_read_b128 v[118:121], v95
	s_waitcnt lgkmcnt(1)
	v_mul_f32_e32 v95, v125, v113
	v_mul_f32_e32 v109, v127, v115
	v_fmac_f32_e32 v95, v124, v112
	v_fmac_f32_e32 v109, v126, v114
	v_add_f32_e32 v95, v95, v109
	v_add_f32_e32 v144, v147, v95
	s_waitcnt lgkmcnt(0)
	v_mul_f32_e32 v95, v125, v119
	v_mul_f32_e32 v109, v127, v121
	v_add_u32_e32 v112, 0x198c0, v153
	v_fmac_f32_e32 v95, v124, v118
	v_fmac_f32_e32 v109, v126, v120
	ds_read_b128 v[112:115], v112
	v_add_f32_e32 v95, v95, v109
	v_add_f32_e32 v145, v160, v95
	v_add_u32_e32 v95, 0x1b8d0, v153
	ds_read_b128 v[118:121], v95
	s_waitcnt lgkmcnt(1)
	v_mul_f32_e32 v95, v125, v113
	v_mul_f32_e32 v109, v127, v115
	v_fmac_f32_e32 v95, v124, v112
	v_fmac_f32_e32 v109, v126, v114
	v_add_f32_e32 v95, v95, v109
	v_add_f32_e32 v147, v140, v95
	s_waitcnt lgkmcnt(0)
	v_mul_f32_e32 v95, v125, v119
	v_mul_f32_e32 v109, v127, v121
	v_add_u32_e32 v112, 0x1d8e0, v153
	v_fmac_f32_e32 v95, v124, v118
	v_fmac_f32_e32 v109, v126, v120
	ds_read_b128 v[112:115], v112
	v_add_f32_e32 v95, v95, v109
	v_add_f32_e32 v160, v141, v95
	v_add_u32_e32 v95, 0x1f8f0, v153
	ds_read_b128 v[118:121], v95
	s_waitcnt lgkmcnt(1)
	v_mul_f32_e32 v95, v125, v113
	v_mul_f32_e32 v109, v127, v115
	v_fmac_f32_e32 v95, v124, v112
	v_fmac_f32_e32 v109, v126, v114
	v_add_f32_e32 v95, v95, v109
	v_add_f32_e32 v146, v146, v95
	s_waitcnt lgkmcnt(0)
	v_mul_f32_e32 v95, v125, v119
	v_mul_f32_e32 v109, v127, v121
	v_fmac_f32_e32 v95, v124, v118
	v_fmac_f32_e32 v109, v126, v120
	v_add_f32_e32 v95, v95, v109
	v_add_f32_e32 v126, v161, v95
	ds_read_b128 v[112:115], v96 offset:7168
	ds_read_b128 v[118:121], v97 offset:7168
	v_add_u32_e32 v124, 0x700, v94
	v_ashrrev_i32_e32 v125, 31, v124
	v_lshl_add_u64 v[94:95], v[124:125], 2, s[12:13]
	v_lshl_add_u64 v[124:125], v[124:125], 1, s[10:11]
	global_load_dwordx2 v[140:141], v[124:125], off nt
	v_pk_mul_f32 v[124:125], v[104:105], v[110:111] op_sel_hi:[1,0]
	v_pk_mul_f32 v[102:103], v[102:103], v[110:111] op_sel_hi:[1,0]
	s_waitcnt lgkmcnt(0)
	v_pk_add_f32 v[118:119], v[118:119], 1.0 op_sel_hi:[1,0]
	v_pk_fma_f32 v[104:105], v[8:9], v[102:103], v[4:5]
	v_pk_fma_f32 v[102:103], v[6:7], v[124:125], v[2:3]
	v_mov_b32_e32 v127, 0
	v_pk_fma_f32 v[118:119], v[102:103], v[118:119], v[112:113]
	v_pk_add_f32 v[120:121], v[120:121], 1.0 op_sel_hi:[1,0]
	v_med3_f32 v110, v118, s29, v151
	v_med3_f32 v112, v119, s29, v151
	v_cvt_pk_fp8_f32 v127, v110, v112
	v_pk_fma_f32 v[120:121], v[104:105], v[120:121], v[114:115]
	global_load_dwordx4 v[94:97], v[94:95], off nt
	v_med3_f32 v110, v120, s29, v151
	v_med3_f32 v112, v121, s29, v151
	v_cvt_pk_fp8_f32 v127, v110, v112 op_sel:[0,0,1]
	v_ashrrev_i32_e32 v109, 31, v108
	v_lshl_add_u64 v[124:125], v[108:109], 2, s[6:7]
	global_store_dwordx4 v[124:125], v[102:105], off nt
	ds_read_b128 v[112:115], v153 offset:7168
	s_nop 0
	v_lshl_add_u64 v[102:103], s[4:5], 0, v[108:109]
	global_store_dword v[102:103], v127, off
	ds_read_b128 v[102:105], v153 offset:15376
	s_waitcnt lgkmcnt(1)
	v_mul_f32_e32 v108, v119, v113
	v_mul_f32_e32 v109, v121, v115
	v_fmac_f32_e32 v108, v118, v112
	v_fmac_f32_e32 v109, v120, v114
	s_waitcnt lgkmcnt(0)
	v_mul_f32_e32 v103, v119, v103
	v_fmac_f32_e32 v103, v118, v102
	v_mul_f32_e32 v102, v121, v105
	ds_read_b128 v[112:115], v153 offset:23584
	v_fmac_f32_e32 v102, v120, v104
	v_add_f32_e32 v102, v103, v102
	v_add_f32_e32 v108, v108, v109
	v_add_f32_e32 v109, v131, v102
	ds_read_b128 v[102:105], v153 offset:31792
	s_waitcnt lgkmcnt(1)
	v_mul_f32_e32 v110, v119, v113
	v_fmac_f32_e32 v110, v118, v112
	v_mul_f32_e32 v112, v121, v115
	v_fmac_f32_e32 v112, v120, v114
	v_add_f32_e32 v110, v110, v112
	s_waitcnt lgkmcnt(0)
	v_mul_f32_e32 v103, v119, v103
	ds_read_b128 v[112:115], v153 offset:40000
	v_fmac_f32_e32 v103, v118, v102
	v_mul_f32_e32 v102, v121, v105
	v_fmac_f32_e32 v102, v120, v104
	v_add_f32_e32 v102, v103, v102
	v_add_f32_e32 v124, v133, v102
	ds_read_b128 v[102:105], v153 offset:48208
	s_waitcnt lgkmcnt(1)
	v_mul_f32_e32 v113, v119, v113
	v_fmac_f32_e32 v113, v118, v112
	v_mul_f32_e32 v112, v121, v115
	v_fmac_f32_e32 v112, v120, v114
	v_add_f32_e32 v112, v113, v112
	v_add_f32_e32 v125, v136, v112
	s_waitcnt lgkmcnt(0)
	v_mul_f32_e32 v103, v119, v103
	ds_read_b128 v[112:115], v153 offset:56416
	v_fmac_f32_e32 v103, v118, v102
	v_mul_f32_e32 v102, v121, v105
	v_fmac_f32_e32 v102, v120, v104
	v_add_f32_e32 v102, v103, v102
	v_add_f32_e32 v127, v137, v102
	ds_read_b128 v[102:105], v153 offset:64624
	s_waitcnt lgkmcnt(1)
	v_mul_f32_e32 v113, v119, v113
	v_fmac_f32_e32 v113, v118, v112
	v_mul_f32_e32 v112, v121, v115
	v_fmac_f32_e32 v112, v120, v114
	v_add_f32_e32 v112, v113, v112
	v_add_f32_e32 v108, v130, v108
	v_add_f32_e32 v130, v138, v112
	s_waitcnt lgkmcnt(0)
	v_mul_f32_e32 v112, v119, v103
	v_fmac_f32_e32 v112, v118, v102
	v_mul_f32_e32 v113, v121, v105
	v_add_u32_e32 v102, 0x11c80, v153
	v_fmac_f32_e32 v113, v120, v104
	ds_read_b128 v[102:105], v102
	v_add_f32_e32 v112, v112, v113
	v_add_f32_e32 v131, v139, v112
	v_add_u32_e32 v112, 0x13c90, v153
	ds_read_b128 v[112:115], v112
	s_waitcnt lgkmcnt(1)
	v_mul_f32_e32 v103, v119, v103
	v_fmac_f32_e32 v103, v118, v102
	v_mul_f32_e32 v102, v121, v105
	v_fmac_f32_e32 v102, v120, v104
	v_add_f32_e32 v102, v103, v102
	s_waitcnt lgkmcnt(0)
	v_mul_f32_e32 v113, v119, v113
	v_add_f32_e32 v110, v132, v110
	v_add_f32_e32 v132, v142, v102
	v_fmac_f32_e32 v113, v118, v112
	v_mul_f32_e32 v112, v121, v115
	v_add_u32_e32 v102, 0x15ca0, v153
	v_fmac_f32_e32 v112, v120, v114
	ds_read_b128 v[102:105], v102
	v_add_f32_e32 v112, v113, v112
	v_add_f32_e32 v133, v143, v112
	v_add_u32_e32 v112, 0x17cb0, v153
	ds_read_b128 v[112:115], v112
	s_waitcnt lgkmcnt(1)
	v_mul_f32_e32 v103, v119, v103
	v_fmac_f32_e32 v103, v118, v102
	v_mul_f32_e32 v102, v121, v105
	v_fmac_f32_e32 v102, v120, v104
	v_add_f32_e32 v102, v103, v102
	s_waitcnt lgkmcnt(0)
	v_mul_f32_e32 v113, v119, v113
	v_add_f32_e32 v136, v144, v102
	v_fmac_f32_e32 v113, v118, v112
	v_mul_f32_e32 v112, v121, v115
	v_add_u32_e32 v102, 0x19cc0, v153
	v_fmac_f32_e32 v112, v120, v114
	ds_read_b128 v[102:105], v102
	v_add_f32_e32 v112, v113, v112
	v_add_f32_e32 v137, v145, v112
	v_add_u32_e32 v112, 0x1bcd0, v153
	ds_read_b128 v[112:115], v112
	s_waitcnt lgkmcnt(1)
	v_mul_f32_e32 v103, v119, v103
	v_fmac_f32_e32 v103, v118, v102
	v_mul_f32_e32 v102, v121, v105
	v_fmac_f32_e32 v102, v120, v104
	v_add_f32_e32 v102, v103, v102
	s_waitcnt lgkmcnt(0)
	v_mul_f32_e32 v113, v119, v113
	v_add_f32_e32 v138, v147, v102
	v_fmac_f32_e32 v113, v118, v112
	v_mul_f32_e32 v112, v121, v115
	v_add_u32_e32 v102, 0x1dce0, v153
	v_fmac_f32_e32 v112, v120, v114
	ds_read_b128 v[102:105], v102
	v_add_f32_e32 v112, v113, v112
	v_add_f32_e32 v139, v160, v112
	v_add_u32_e32 v112, 0x1fcf0, v153
	ds_read_b128 v[112:115], v112
	s_waitcnt lgkmcnt(1)
	v_mul_f32_e32 v103, v119, v103
	v_fmac_f32_e32 v103, v118, v102
	v_mul_f32_e32 v102, v121, v105
	v_fmac_f32_e32 v102, v120, v104
	v_add_f32_e32 v102, v103, v102
	s_waitcnt lgkmcnt(0)
	v_mul_f32_e32 v103, v119, v113
	v_mul_f32_e32 v104, v121, v115
	v_fmac_f32_e32 v103, v118, v112
	v_fmac_f32_e32 v104, v120, v114
	v_add_f32_e32 v103, v103, v104
	v_add_f32_e32 v102, v146, v102
	v_add_f32_e32 v103, v126, v103
	v_and_b32_e32 v104, 32, v152
	v_cmp_eq_u32_e32 vcc, 0, v104
	v_and_b32_e32 v115, 16, v152
	v_cmp_eq_u32_e64 s[0:1], 0, v115
	v_cndmask_b32_e32 v105, v108, v132, vcc
	v_cndmask_b32_e32 v104, v132, v108, vcc
	ds_bpermute_b32 v105, v154, v105
	v_cndmask_b32_e32 v108, v109, v133, vcc
	ds_bpermute_b32 v108, v154, v108
	v_cndmask_b32_e32 v112, v110, v136, vcc
	ds_bpermute_b32 v112, v154, v112
	s_waitcnt lgkmcnt(2)
	v_add_f32_e32 v104, v104, v105
	v_cndmask_b32_e32 v105, v133, v109, vcc
	s_waitcnt lgkmcnt(1)
	v_add_f32_e32 v105, v105, v108
	v_cndmask_b32_e32 v108, v136, v110, vcc
	v_cndmask_b32_e32 v110, v124, v137, vcc
	s_waitcnt lgkmcnt(0)
	v_add_f32_e32 v108, v108, v112
	ds_bpermute_b32 v110, v154, v110
	v_cndmask_b32_e32 v112, v125, v138, vcc
	ds_bpermute_b32 v112, v154, v112
	v_cndmask_b32_e32 v113, v127, v139, vcc
	ds_bpermute_b32 v113, v154, v113
	v_cndmask_b32_e32 v109, v137, v124, vcc
	s_waitcnt lgkmcnt(2)
	v_add_f32_e32 v109, v109, v110
	v_cndmask_b32_e32 v110, v138, v125, vcc
	s_waitcnt lgkmcnt(1)
	v_add_f32_e32 v110, v110, v112
	v_cndmask_b32_e32 v112, v139, v127, vcc
	s_waitcnt lgkmcnt(0)
	v_add_f32_e32 v112, v112, v113
	v_cndmask_b32_e32 v113, v130, v102, vcc
	v_cndmask_b32_e32 v114, v131, v103, vcc
	ds_bpermute_b32 v113, v154, v113
	ds_bpermute_b32 v114, v154, v114
	v_cndmask_b32_e32 v102, v102, v130, vcc
	v_cndmask_b32_e32 v103, v103, v131, vcc
	v_cndmask_b32_e64 v115, v110, v104, s[0:1]
	s_waitcnt lgkmcnt(1)
	v_add_f32_e32 v102, v102, v113
	s_waitcnt lgkmcnt(0)
	v_add_f32_e32 v103, v103, v114
	v_cndmask_b32_e64 v104, v104, v110, s[0:1]
	v_cndmask_b32_e64 v110, v112, v105, s[0:1]
	v_cndmask_b32_e64 v105, v105, v112, s[0:1]
	v_cndmask_b32_e64 v112, v108, v102, s[0:1]
	v_cndmask_b32_e64 v113, v109, v103, s[0:1]
	ds_bpermute_b32 v104, v155, v104
	ds_bpermute_b32 v105, v155, v105
	ds_bpermute_b32 v112, v155, v112
	ds_bpermute_b32 v113, v155, v113
	v_cndmask_b32_e64 v102, v102, v108, s[0:1]
	v_cndmask_b32_e64 v103, v103, v109, s[0:1]
	v_and_b32_e32 v108, 8, v152
	s_waitcnt lgkmcnt(3)
	v_add_f32_e32 v104, v115, v104
	s_waitcnt lgkmcnt(2)
	v_add_f32_e32 v105, v110, v105
	s_waitcnt lgkmcnt(1)
	v_add_f32_e32 v102, v102, v112
	s_waitcnt lgkmcnt(0)
	v_add_f32_e32 v103, v103, v113
	v_cmp_eq_u32_e32 vcc, 0, v108
	s_nop 1
	v_cndmask_b32_e32 v108, v102, v104, vcc
	v_cndmask_b32_e32 v102, v104, v102, vcc
	v_cndmask_b32_e32 v104, v105, v103, vcc
	ds_bpermute_b32 v104, v156, v104
	ds_bpermute_b32 v102, v156, v102
	v_cndmask_b32_e32 v103, v103, v105, vcc
	v_and_b32_e32 v105, 3, v152
	s_waitcnt lgkmcnt(1)
	v_add_f32_e32 v103, v103, v104
	v_and_b32_e32 v104, 4, v152
	s_waitcnt lgkmcnt(0)
	v_add_f32_e32 v102, v108, v102
	v_cmp_eq_u32_e32 vcc, 0, v104
	s_nop 1
	v_cndmask_b32_e32 v104, v103, v102, vcc
	v_cndmask_b32_e32 v102, v102, v103, vcc
	ds_bpermute_b32 v102, v157, v102
	v_cmp_eq_u32_e32 vcc, 0, v105
	s_waitcnt lgkmcnt(0)
	v_add_f32_e32 v102, v104, v102
	ds_bpermute_b32 v103, v158, v102
	s_waitcnt lgkmcnt(0)
	v_add_f32_e32 v102, v102, v103
	ds_bpermute_b32 v103, v159, v102
	s_waitcnt lgkmcnt(0)
	v_add_f32_e32 v102, v102, v103
	ds_bpermute_b32 v103, v154, v102
	s_waitcnt lgkmcnt(0)
	v_max_f32_e32 v103, v103, v103
	v_max_f32_e32 v103, v102, v103
	ds_bpermute_b32 v104, v155, v103
	s_waitcnt lgkmcnt(0)
	v_max_f32_e32 v104, v104, v104
	v_max_f32_e32 v103, v103, v104
	ds_bpermute_b32 v104, v156, v103
	s_waitcnt lgkmcnt(0)
	v_max_f32_e32 v104, v104, v104
	v_max_f32_e32 v103, v103, v104
	ds_bpermute_b32 v104, v157, v103
	s_waitcnt lgkmcnt(0)
	v_max_f32_e32 v104, v104, v104
	v_max_f32_e32 v103, v103, v104
	ds_bpermute_b32 v104, v158, v103
	s_waitcnt lgkmcnt(0)
	v_max_f32_e32 v104, v104, v104
	v_max_f32_e32 v103, v103, v104
	ds_bpermute_b32 v104, v159, v103
	s_waitcnt lgkmcnt(0)
	v_max_f32_e32 v104, v104, v104
	v_max_f32_e32 v103, v103, v104
	v_sub_f32_e32 v102, v102, v103
	v_mul_f32_e32 v102, 0x3fb8aa3b, v102
	v_exp_f32_e32 v102, v102
	ds_bpermute_b32 v103, v154, v102
	s_waitcnt lgkmcnt(0)
	v_add_f32_e32 v103, v102, v103
	ds_bpermute_b32 v104, v155, v103
	s_waitcnt lgkmcnt(0)
	v_add_f32_e32 v103, v103, v104
	ds_bpermute_b32 v104, v156, v103
	s_waitcnt lgkmcnt(0)
	v_add_f32_e32 v103, v103, v104
	ds_bpermute_b32 v104, v157, v103
	s_waitcnt lgkmcnt(0)
	v_add_f32_e32 v103, v103, v104
	ds_bpermute_b32 v104, v158, v103
	s_waitcnt lgkmcnt(0)
	v_add_f32_e32 v103, v103, v104
	ds_bpermute_b32 v104, v159, v103
	s_and_saveexec_b64 s[0:1], vcc
	s_cbranch_execz .LBB0_779
	s_waitcnt lgkmcnt(0)
	v_add_f32_e32 v103, v103, v104
	v_mul_f32_e32 v103, 0x3e800000, v103
	v_div_scale_f32 v104, s[34:35], v103, v103, v102
	v_rcp_f32_e32 v105, v104
	v_bfe_u32 v108, v152, 2, 4
	v_fma_f32 v109, -v104, v105, 1.0
	v_fmac_f32_e32 v105, v109, v105
	v_div_scale_f32 v109, vcc, v102, v103, v102
	v_mul_f32_e32 v110, v109, v105
	v_fma_f32 v112, -v104, v110, v109
	v_fmac_f32_e32 v110, v112, v105
	v_fma_f32 v104, -v104, v110, v109
	v_div_fmas_f32 v104, v104, v105, v110
	v_div_fixup_f32 v109, v104, v103, v102
	v_add_u32_e32 v102, s31, v108
	v_ashrrev_i32_e32 v103, 31, v102
	v_lshlrev_b64 v[102:103], 2, v[102:103]
	v_lshl_add_u64 v[104:105], s[14:15], 0, v[102:103]
	v_lshl_add_u64 v[102:103], s[8:9], 0, v[102:103]
	global_store_dword v[104:105], v109, off
	global_store_dword v[102:103], v149, off
	s_branch .LBB0_779
